# MoE down GEMM runs on the XCD that produced its rows (group g on XCD g%8, leftover groups to XCD 7-j); gate/up rows consumed on the same verified XCD are stored plain into the shared L2 instead of wri
# speedup vs baseline: 1.0036x; 1.0030x over previous
;     __device__ __forceinline__ bool next(int i, Unit& u) const {
;         const int T = __builtin_amdgcn_readfirstlane(moe[16]), Ng = (T + 7) >> 3, x = c & 7, k = c >> 3; int g;
;         if (TOKEN_ROWS) g = x + 8 * i;
;         else { const int hc = Ng & 7, nl = 8 - hc;
;             if (x >= hc) g = i == 0 ? x - hc : nl + (i - 1) * 8 + (x - hc); else g = 2 * nl + 8 * i + x; }
;         if (g >= Ng) return false;
.LBB0_1596:
	v_readlane_b32 s4, v254, 37
	s_add_i32 s58, s58, 1
	s_mov_b64 s[30:31], 0
	v_mov_b32_e32 v0, s4
	ds_read_b32 v0, v0
	s_lshl_b32 s4, s58, 3
	s_or_b32 s4, s4, s42
	s_waitcnt lgkmcnt(0)
	v_readfirstlane_b32 s5, v0
	s_add_i32 s7, s5, 7
	s_ashr_i32 s7, s7, 3
	v_readlane_b32 s101, v254, 28
	s_lshr_b32 s100, s7, 3
	s_nop 0
	v_mov_b32_e32 v1, s101
	ds_read_b32 v1, v1
	s_cmp_le_u32 s58, s100
	s_cselect_b32 s100, 1, 0
	s_waitcnt lgkmcnt(0)
	v_readfirstlane_b32 s101, v1
	s_and_b32 s101, s101, s100
	s_cmp_ge_i32 s4, s7
	s_cbranch_scc1 .LBB0_1599
	s_lshl_b32 s4, s4, 3
	s_add_i32 s4, s4, s57
	s_cmp_ge_i32 s4, s5
	s_cbranch_scc1 .LBB0_1599
	v_readlane_b32 s5, v254, 29
	s_mov_b64 s[30:31], -1
	s_nop 0
	v_mov_b32_e32 v0, s5
	ds_read_b128 v[16:19], v0
	ds_read_b128 v[20:23], v0 offset:16
	ds_read_b128 v[24:27], v0 offset:32
	ds_read_b128 v[28:31], v0 offset:48
	s_mov_b32 s24, 0
	s_waitcnt lgkmcnt(0)
	v_readfirstlane_b32 s5, v17
	s_cmp_ge_i32 s4, s5
	s_addc_u32 s24, s24, 0
	v_readfirstlane_b32 s5, v18
	s_cmp_ge_i32 s4, s5
	s_addc_u32 s24, s24, 0
	v_readfirstlane_b32 s5, v19
	s_cmp_ge_i32 s4, s5
	s_addc_u32 s24, s24, 0
	v_readfirstlane_b32 s5, v20
	s_cmp_ge_i32 s4, s5
	s_addc_u32 s24, s24, 0
	v_readfirstlane_b32 s5, v21
	s_cmp_ge_i32 s4, s5
	s_addc_u32 s24, s24, 0
	v_readfirstlane_b32 s5, v22
	s_cmp_ge_i32 s4, s5
	s_addc_u32 s24, s24, 0
	v_readfirstlane_b32 s5, v23
	s_cmp_ge_i32 s4, s5
	s_addc_u32 s24, s24, 0
	v_readfirstlane_b32 s5, v24
	s_cmp_ge_i32 s4, s5
	s_addc_u32 s24, s24, 0
	v_readfirstlane_b32 s5, v25
	s_cmp_ge_i32 s4, s5
	s_addc_u32 s24, s24, 0
	v_readfirstlane_b32 s5, v26
	s_cmp_ge_i32 s4, s5
	s_addc_u32 s24, s24, 0
	v_readfirstlane_b32 s5, v27
	s_cmp_ge_i32 s4, s5
	s_addc_u32 s24, s24, 0
	v_readfirstlane_b32 s5, v28
	s_cmp_ge_i32 s4, s5
	s_addc_u32 s24, s24, 0
	v_readfirstlane_b32 s5, v29
	s_cmp_ge_i32 s4, s5
	s_addc_u32 s24, s24, 0
	v_readfirstlane_b32 s5, v30
	s_cmp_ge_i32 s4, s5
	s_addc_u32 s24, s24, 0
	v_readfirstlane_b32 s5, v31
	s_cmp_ge_i32 s4, s5
	s_addc_u32 s24, s24, 0
	s_lshl_b32 s5, s24, 2
	s_addk_i32 s5, 0x100
	s_add_i32 s5, s5, 0x20040
	v_mov_b32_e32 v0, s5
	ds_read2_b32 v[0:1], v0 offset1:17
	s_waitcnt lgkmcnt(0)
	v_sub_u32_e32 v0, s4, v0
	s_nop 0
	v_readfirstlane_b32 s60, v0
	v_readfirstlane_b32 s4, v1
	s_lshl_b32 s5, s60, 8
	s_sub_i32 s4, s4, s5
	s_min_i32 s61, s4, 0x100

; __device__ __forceinline__ unsigned cvt_pk_bf16(float lo, float hi) { unsigned r; asm volatile("v_cvt_pk_bf16_f32 %0, %1, %2" : "=v"(r) : "v"(lo), "v"(hi)); return r; }
; __device__ __forceinline__ void st_wt16(void* p, u32x4 v) { asm volatile("global_store_dwordx4 %0, %1, off sc1\n\ts_nop 1" :: "v"(p), "v"(v) : "memory"); }
;     __device__ __forceinline__ void operator()(const f32x4 (&acc)[2][2][4][2], const Unit& u, int wr, int wc, int fr, int fq) const {
;     ...
;         for (int j = 0; j < 8; ++j) { const int r = (j >> 2) * HALF + wr * 64 + (j & 3) * 16 + fr; slots[j] = list[u.e * LCAP + u.pm * BM + (r < u.rows ? r : u.rows - 1)]; }
; #pragma unroll
;         for (int j = 0; j < 8; ++j) { scv[j] = rsc ? rsc[slots[j]] * cs : cs; gwv[j] = gatew[slots[j]]; }
; #pragma unroll
;         for (int ai = 0; ai < 2; ++ai)
; #pragma unroll
;             for (int m = 0; m < 4; ++m) {
;                 const int r = ai * HALF + wr * 64 + m * 16 + fr; const bool valid = r < u.rows;
;                 const int slot = slots[ai * 4 + m];
;                 const float sc = scv[ai * 4 + m], gw = gwv[ai * 4 + m]; float o[8];
; #pragma unroll
;                 for (int n = 0; n < 2; ++n) { const f32x4 g = acc[ai][0][m][n] * sc, up = acc[ai][1][m][n] * sc;
; #pragma unroll
;                     for (int j = 0; j < 4; ++j) o[4 * n + j] = g[j] * __builtin_amdgcn_rcpf(1.0f + __expf(-g[j])) * up[j] * gw; }
;                 u32x4 w; w.x = cvt_pk_bf16(o[0], o[1]); w.y = cvt_pk_bf16(o[2], o[3]); w.z = cvt_pk_bf16(o[4], o[5]); w.w = cvt_pk_bf16(o[6], o[7]);
;                 if (valid) st_wt16(hid + (size_t)slot * 512 + f0, w);
.LBB0_1605:
	v_mbcnt_lo_u32_b32 v64, -1, 0
	v_mbcnt_hi_u32_b32 v64, -1, v64
	s_lshl_b32 s0, s6, 14
	v_add_u32_e32 v130, s93, v64
	s_lshl_b32 s1, s33, 8
	v_and_b32_e32 v64, 15, v130
	s_add_i32 s0, s0, s1
	s_add_i32 s1, s40, -1
	v_or_b32_e32 v156, s49, v64
	v_bfe_u32 v155, v130, 4, 2
	v_min_i32_e32 v130, s1, v156
	v_add_u32_e32 v130, s0, v130
	v_ashrrev_i32_e32 v131, 31, v130
	v_lshl_add_u64 v[130:131], v[130:131], 2, s[12:13]
	global_load_dword v152, v[130:131], off
	v_or_b32_e32 v165, 16, v156
	v_min_i32_e32 v130, s1, v165
	v_add_u32_e32 v130, s0, v130
	v_ashrrev_i32_e32 v131, 31, v130
	v_lshl_add_u64 v[130:131], v[130:131], 2, s[12:13]
	v_or_b32_e32 v163, 32, v156
	global_load_dword v144, v[130:131], off
	v_min_i32_e32 v130, s1, v163
	v_add_u32_e32 v130, s0, v130
	v_ashrrev_i32_e32 v131, 31, v130
	v_lshl_add_u64 v[130:131], v[130:131], 2, s[12:13]
	v_or_b32_e32 v161, 48, v156
	global_load_dword v142, v[130:131], off
	v_min_i32_e32 v130, s1, v161
	v_add_u32_e32 v130, s0, v130
	v_ashrrev_i32_e32 v131, 31, v130
	v_lshl_add_u64 v[130:131], v[130:131], 2, s[12:13]
	v_or_b32_e32 v132, s56, v64
	global_load_dword v140, v[130:131], off
	v_min_i32_e32 v130, s1, v132
	v_add_u32_e32 v130, s0, v130
	v_ashrrev_i32_e32 v131, 31, v130
	v_lshl_add_u64 v[130:131], v[130:131], 2, s[12:13]
	global_load_dword v138, v[130:131], off
	v_or_b32_e32 v130, 16, v132
	v_min_i32_e32 v130, s1, v130
	v_add_u32_e32 v130, s0, v130
	v_ashrrev_i32_e32 v131, 31, v130
	v_lshl_add_u64 v[130:131], v[130:131], 2, s[12:13]
	global_load_dword v136, v[130:131], off
	v_or_b32_e32 v130, 32, v132
	v_min_i32_e32 v130, s1, v130
	v_add_u32_e32 v130, s0, v130
	v_ashrrev_i32_e32 v131, 31, v130
	v_lshl_add_u64 v[130:131], v[130:131], 2, s[12:13]
	global_load_dword v134, v[130:131], off
	v_or_b32_e32 v130, 48, v132
	v_min_i32_e32 v130, s1, v130
	v_add_u32_e32 v130, s0, v130
	v_ashrrev_i32_e32 v131, 31, v130
	v_lshl_add_u64 v[130:131], v[130:131], 2, s[12:13]
	global_load_dword v130, v[130:131], off
	v_mul_f32_e32 v126, 0x3c800000, v126
	v_mul_f32_e32 v147, 0xbfb8aa3b, v126
	v_exp_f32_e32 v147, v147
	v_mul_f32_e32 v122, 0x3c800000, v122
	v_mul_f32_e32 v123, 0x3c800000, v123
	v_mul_f32_e32 v124, 0x3c800000, v124
	v_add_f32_e32 v147, 1.0, v147
	v_rcp_f32_e32 v147, v147
	v_mul_f32_e32 v125, 0x3c800000, v125
	v_mul_f32_e32 v118, 0x3c800000, v118
	v_mul_f32_e32 v114, 0x3c800000, v114
	v_mul_f32_e32 v126, v126, v147
	v_mul_f32_e32 v122, v126, v122
	v_mul_f32_e32 v126, 0x3c800000, v127
	v_mul_f32_e32 v127, 0xbfb8aa3b, v126
	v_exp_f32_e32 v127, v127
	v_mul_f32_e32 v115, 0x3c800000, v115
	s_lshl_b32 s0, s28, 7
	v_cmp_gt_i32_e32 vcc, s40, v156
	v_add_f32_e32 v127, 1.0, v127
	v_rcp_f32_e32 v127, v127
	s_waitcnt vmcnt(0)
	v_ashrrev_i32_e32 v153, 31, v152
	v_lshl_add_u64 v[132:133], v[152:153], 2, s[16:17]
	global_load_dword v146, v[132:133], off
	v_mul_f32_e32 v126, v126, v127
	v_mul_f32_e32 v123, v126, v123
	v_mul_f32_e32 v126, 0x3c800000, v128
	v_mul_f32_e32 v127, 0xbfb8aa3b, v126
	v_ashrrev_i32_e32 v145, 31, v144
	v_lshl_add_u64 v[132:133], v[144:145], 2, s[16:17]
	global_load_dword v166, v[132:133], off
	v_exp_f32_e32 v127, v127
	v_ashrrev_i32_e32 v143, 31, v142
	v_lshl_add_u64 v[132:133], v[142:143], 2, s[16:17]
	global_load_dword v164, v[132:133], off
	v_add_f32_e32 v127, 1.0, v127
	v_rcp_f32_e32 v127, v127
	v_ashrrev_i32_e32 v141, 31, v140
	v_lshl_add_u64 v[132:133], v[140:141], 2, s[16:17]
	global_load_dword v162, v[132:133], off
	v_mul_f32_e32 v126, v126, v127
	v_mul_f32_e32 v124, v126, v124
	v_ashrrev_i32_e32 v139, 31, v138
	v_lshl_add_u64 v[132:133], v[138:139], 2, s[16:17]
	global_load_dword v160, v[132:133], off
	v_mul_f32_e32 v126, 0x3c800000, v129
	v_mul_f32_e32 v127, 0xbfb8aa3b, v126
	v_exp_f32_e32 v127, v127
	v_ashrrev_i32_e32 v137, 31, v136
	v_lshl_add_u64 v[132:133], v[136:137], 2, s[16:17]
	global_load_dword v159, v[132:133], off
	v_add_f32_e32 v127, 1.0, v127
	v_rcp_f32_e32 v127, v127
	v_ashrrev_i32_e32 v135, 31, v134
	v_lshl_add_u64 v[132:133], v[134:135], 2, s[16:17]
	global_load_dword v158, v[132:133], off
	v_mul_f32_e32 v126, v126, v127
	v_mul_f32_e32 v125, v126, v125
	v_mul_f32_e32 v126, 0xbfb8aa3b, v118
	v_ashrrev_i32_e32 v131, 31, v130
	v_lshl_add_u64 v[132:133], v[130:131], 2, s[16:17]
	global_load_dword v157, v[132:133], off
	v_exp_f32_e32 v126, v126
	v_lshl_or_b32 v132, v155, 3, s0
	v_or_b32_e32 v132, s50, v132
	v_ashrrev_i32_e32 v133, 31, v132
	v_add_f32_e32 v126, 1.0, v126
	v_rcp_f32_e32 v126, v126
	s_waitcnt vmcnt(7)
	v_mul_f32_e32 v122, v122, v146
	v_mul_f32_e32 v118, v118, v126
	v_mul_f32_e32 v114, v118, v114
	v_mul_f32_e32 v118, v114, v146
	v_mul_f32_e32 v114, 0x3c800000, v119
	v_mul_f32_e32 v119, 0xbfb8aa3b, v114
	v_exp_f32_e32 v119, v119
	v_mul_f32_e32 v123, v123, v146
	v_mul_f32_e32 v124, v124, v146
	v_mul_f32_e32 v125, v125, v146
	v_add_f32_e32 v119, 1.0, v119
	v_rcp_f32_e32 v119, v119
	s_nop 0
	v_mul_f32_e32 v114, v114, v119
	v_mul_f32_e32 v114, v114, v115
	v_mul_f32_e32 v119, v114, v146
	v_mul_f32_e32 v114, 0x3c800000, v120
	v_mul_f32_e32 v115, 0xbfb8aa3b, v114
	v_exp_f32_e32 v115, v115
	s_nop 0
	v_add_f32_e32 v115, 1.0, v115
	v_rcp_f32_e32 v115, v115
	s_nop 0
	v_mul_f32_e32 v114, v114, v115
	v_mul_f32_e32 v115, 0x3c800000, v116
	v_mul_f32_e32 v114, v114, v115
	v_mul_f32_e32 v120, v114, v146
	v_mul_f32_e32 v114, 0x3c800000, v121
	v_mul_f32_e32 v115, 0xbfb8aa3b, v114
	v_exp_f32_e32 v115, v115
	s_nop 0
	v_add_f32_e32 v115, 1.0, v115
	v_rcp_f32_e32 v115, v115
	s_nop 0
	v_mul_f32_e32 v114, v114, v115
	v_mul_f32_e32 v115, 0x3c800000, v117
	v_mul_f32_e32 v114, v114, v115
	v_mul_f32_e32 v117, v114, v146
	v_cvt_pk_bf16_f32 v114, v122, v123
	v_cvt_pk_bf16_f32 v115, v124, v125
	v_cvt_pk_bf16_f32 v116, v118, v119
	v_cvt_pk_bf16_f32 v117, v120, v117
	s_and_saveexec_b64 s[0:1], vcc
	s_cbranch_execz .LBB0_1607
	v_lshlrev_b64 v[118:119], 10, v[152:153]
	v_lshl_add_u64 v[118:119], s[10:11], 0, v[118:119]
	v_lshl_add_u64 v[118:119], v[132:133], 1, v[118:119]
	s_cmp_lg_u32 s101, 0
	s_cbranch_scc1 .Lm1pl_0
	global_store_dwordx4 v[118:119], v[114:117], off sc1
	s_branch .Lm1dn_0
; __device__ __forceinline__ unsigned cvt_pk_bf16(float lo, float hi) { unsigned r; asm volatile("v_cvt_pk_bf16_f32 %0, %1, %2" : "=v"(r) : "v"(lo), "v"(hi)); return r; }
; __device__ __forceinline__ void st_wt16(void* p, u32x4 v) { asm volatile("global_store_dwordx4 %0, %1, off sc1\n\ts_nop 1" :: "v"(p), "v"(v) : "memory"); }
;     __device__ __forceinline__ void operator()(const f32x4 (&acc)[2][2][4][2], const Unit& u, int wr, int wc, int fr, int fq) const {
;     ...
;                 const int r = ai * HALF + wr * 64 + m * 16 + fr; const bool valid = r < u.rows;
;                 const int slot = slots[ai * 4 + m];
;                 const float sc = scv[ai * 4 + m], gw = gwv[ai * 4 + m]; float o[8];
; #pragma unroll
;                 for (int n = 0; n < 2; ++n) { const f32x4 g = acc[ai][0][m][n] * sc, up = acc[ai][1][m][n] * sc;
; #pragma unroll
;                     for (int j = 0; j < 4; ++j) o[4 * n + j] = g[j] * __builtin_amdgcn_rcpf(1.0f + __expf(-g[j])) * up[j] * gw; }
;                 u32x4 w; w.x = cvt_pk_bf16(o[0], o[1]); w.y = cvt_pk_bf16(o[2], o[3]); w.z = cvt_pk_bf16(o[4], o[5]); w.w = cvt_pk_bf16(o[6], o[7]);
;                 if (valid) st_wt16(hid + (size_t)slot * 512 + f0, w);
.Lm1pl_0:
	global_store_dwordx4 v[118:119], v[114:117], off
.Lm1dn_0:
	s_nop 1
.LBB0_1607:
	s_or_b64 exec, exec, s[0:1]
	v_mul_f32_e32 v110, 0x3c800000, v110
	v_mul_f32_e32 v114, 0xbfb8aa3b, v110
	v_exp_f32_e32 v114, v114
	v_mul_f32_e32 v106, 0x3c800000, v106
	v_mul_f32_e32 v107, 0x3c800000, v107
	v_mul_f32_e32 v108, 0x3c800000, v108
	v_add_f32_e32 v114, 1.0, v114
	v_rcp_f32_e32 v114, v114
	v_mul_f32_e32 v109, 0x3c800000, v109
	v_mul_f32_e32 v102, 0x3c800000, v102
	v_mul_f32_e32 v98, 0x3c800000, v98
	v_mul_f32_e32 v110, v110, v114
	v_mul_f32_e32 v106, v110, v106
	v_mul_f32_e32 v110, 0x3c800000, v111
	v_mul_f32_e32 v111, 0xbfb8aa3b, v110
	v_exp_f32_e32 v111, v111
	v_mul_f32_e32 v99, 0x3c800000, v99
	v_cmp_gt_i32_e32 vcc, s40, v165
	s_waitcnt vmcnt(6)
	v_mul_f32_e32 v106, v106, v166
	v_add_f32_e32 v111, 1.0, v111
	v_rcp_f32_e32 v111, v111
	s_nop 0
	v_mul_f32_e32 v110, v110, v111
	v_mul_f32_e32 v107, v110, v107
	v_mul_f32_e32 v110, 0x3c800000, v112
	v_mul_f32_e32 v111, 0xbfb8aa3b, v110
	v_exp_f32_e32 v111, v111
	v_mul_f32_e32 v107, v107, v166
	v_add_f32_e32 v111, 1.0, v111
	v_rcp_f32_e32 v111, v111
	s_nop 0
	v_mul_f32_e32 v110, v110, v111
	v_mul_f32_e32 v108, v110, v108
	v_mul_f32_e32 v110, 0x3c800000, v113
	v_mul_f32_e32 v111, 0xbfb8aa3b, v110
	v_exp_f32_e32 v111, v111
	v_mul_f32_e32 v108, v108, v166
	v_add_f32_e32 v111, 1.0, v111
	v_rcp_f32_e32 v111, v111
	s_nop 0
	v_mul_f32_e32 v110, v110, v111
	v_mul_f32_e32 v109, v110, v109
	v_mul_f32_e32 v110, 0xbfb8aa3b, v102
	v_exp_f32_e32 v110, v110
	v_mul_f32_e32 v109, v109, v166
	v_add_f32_e32 v110, 1.0, v110
	v_rcp_f32_e32 v110, v110
	s_nop 0
	v_mul_f32_e32 v102, v102, v110
	v_mul_f32_e32 v98, v102, v98
	v_mul_f32_e32 v102, v98, v166
	v_mul_f32_e32 v98, 0x3c800000, v103
	v_mul_f32_e32 v103, 0xbfb8aa3b, v98
	v_exp_f32_e32 v103, v103
	s_nop 0
	v_add_f32_e32 v103, 1.0, v103
	v_rcp_f32_e32 v103, v103
	s_nop 0
	v_mul_f32_e32 v98, v98, v103
	v_mul_f32_e32 v98, v98, v99
	v_mul_f32_e32 v103, v98, v166
	v_mul_f32_e32 v98, 0x3c800000, v104
	v_mul_f32_e32 v99, 0xbfb8aa3b, v98
	v_exp_f32_e32 v99, v99
	s_nop 0
	v_add_f32_e32 v99, 1.0, v99
	v_rcp_f32_e32 v99, v99
	s_nop 0
	v_mul_f32_e32 v98, v98, v99
	v_mul_f32_e32 v99, 0x3c800000, v100
	v_mul_f32_e32 v98, v98, v99
	v_mul_f32_e32 v104, v98, v166
	v_mul_f32_e32 v98, 0x3c800000, v105
	v_mul_f32_e32 v99, 0xbfb8aa3b, v98
	v_exp_f32_e32 v99, v99
	s_nop 0
	v_add_f32_e32 v99, 1.0, v99
	v_rcp_f32_e32 v99, v99
	s_nop 0
	v_mul_f32_e32 v98, v98, v99
	v_mul_f32_e32 v99, 0x3c800000, v101
	v_mul_f32_e32 v98, v98, v99
	v_mul_f32_e32 v101, v98, v166
	v_cvt_pk_bf16_f32 v98, v106, v107
	v_cvt_pk_bf16_f32 v99, v108, v109
	v_cvt_pk_bf16_f32 v100, v102, v103
	v_cvt_pk_bf16_f32 v101, v104, v101
	s_and_saveexec_b64 s[0:1], vcc
	s_cbranch_execz .LBB0_1609
	v_lshlrev_b64 v[102:103], 10, v[144:145]
	v_lshl_add_u64 v[102:103], s[10:11], 0, v[102:103]
	v_lshl_add_u64 v[102:103], v[132:133], 1, v[102:103]
	s_cmp_lg_u32 s101, 0
	s_cbranch_scc1 .Lm1pl_1
	global_store_dwordx4 v[102:103], v[98:101], off sc1
	s_branch .Lm1dn_1
.Lm1pl_1:
	global_store_dwordx4 v[102:103], v[98:101], off

; __device__ __forceinline__ unsigned cvt_pk_bf16(float lo, float hi) { unsigned r; asm volatile("v_cvt_pk_bf16_f32 %0, %1, %2" : "=v"(r) : "v"(lo), "v"(hi)); return r; }
; __device__ __forceinline__ void st_wt16(void* p, u32x4 v) { asm volatile("global_store_dwordx4 %0, %1, off sc1\n\ts_nop 1" :: "v"(p), "v"(v) : "memory"); }
;     __device__ __forceinline__ void operator()(const f32x4 (&acc)[2][2][4][2], const Unit& u, int wr, int wc, int fr, int fq) const {
;     ...
;                 const int r = ai * HALF + wr * 64 + m * 16 + fr; const bool valid = r < u.rows;
;                 const int slot = slots[ai * 4 + m];
;                 const float sc = scv[ai * 4 + m], gw = gwv[ai * 4 + m]; float o[8];
; #pragma unroll
;                 for (int n = 0; n < 2; ++n) { const f32x4 g = acc[ai][0][m][n] * sc, up = acc[ai][1][m][n] * sc;
; #pragma unroll
;                     for (int j = 0; j < 4; ++j) o[4 * n + j] = g[j] * __builtin_amdgcn_rcpf(1.0f + __expf(-g[j])) * up[j] * gw; }
;                 u32x4 w; w.x = cvt_pk_bf16(o[0], o[1]); w.y = cvt_pk_bf16(o[2], o[3]); w.z = cvt_pk_bf16(o[4], o[5]); w.w = cvt_pk_bf16(o[6], o[7]);
;                 if (valid) st_wt16(hid + (size_t)slot * 512 + f0, w);
.LBB0_1609:
	s_or_b64 exec, exec, s[0:1]
	v_mul_f32_e32 v94, 0x3c800000, v94
	v_mul_f32_e32 v98, 0xbfb8aa3b, v94
	v_exp_f32_e32 v98, v98
	v_mul_f32_e32 v90, 0x3c800000, v90
	v_mul_f32_e32 v91, 0x3c800000, v91
	v_mul_f32_e32 v92, 0x3c800000, v92
	v_add_f32_e32 v98, 1.0, v98
	v_rcp_f32_e32 v98, v98
	v_mul_f32_e32 v93, 0x3c800000, v93
	v_mul_f32_e32 v86, 0x3c800000, v86
	v_mul_f32_e32 v82, 0x3c800000, v82
	v_mul_f32_e32 v94, v94, v98
	v_mul_f32_e32 v90, v94, v90
	v_mul_f32_e32 v94, 0x3c800000, v95
	v_mul_f32_e32 v95, 0xbfb8aa3b, v94
	v_exp_f32_e32 v95, v95
	v_mul_f32_e32 v83, 0x3c800000, v83
	s_waitcnt vmcnt(5)
	v_mul_f32_e32 v90, v90, v164
	v_cmp_gt_i32_e32 vcc, s40, v163
	v_add_f32_e32 v95, 1.0, v95
	v_rcp_f32_e32 v95, v95
	s_nop 0
	v_mul_f32_e32 v94, v94, v95
	v_mul_f32_e32 v91, v94, v91
	v_mul_f32_e32 v94, 0x3c800000, v96
	v_mul_f32_e32 v95, 0xbfb8aa3b, v94
	v_exp_f32_e32 v95, v95
	v_mul_f32_e32 v91, v91, v164
	v_add_f32_e32 v95, 1.0, v95
	v_rcp_f32_e32 v95, v95
	s_nop 0
	v_mul_f32_e32 v94, v94, v95
	v_mul_f32_e32 v92, v94, v92
	v_mul_f32_e32 v94, 0x3c800000, v97
	v_mul_f32_e32 v95, 0xbfb8aa3b, v94
	v_exp_f32_e32 v95, v95
	v_mul_f32_e32 v92, v92, v164
	v_add_f32_e32 v95, 1.0, v95
	v_rcp_f32_e32 v95, v95
	s_nop 0
	v_mul_f32_e32 v94, v94, v95
	v_mul_f32_e32 v93, v94, v93
	v_mul_f32_e32 v94, 0xbfb8aa3b, v86
	v_exp_f32_e32 v94, v94
	v_mul_f32_e32 v93, v93, v164
	v_add_f32_e32 v94, 1.0, v94
	v_rcp_f32_e32 v94, v94
	s_nop 0
	v_mul_f32_e32 v86, v86, v94
	v_mul_f32_e32 v82, v86, v82
	v_mul_f32_e32 v86, v82, v164
	v_mul_f32_e32 v82, 0x3c800000, v87
	v_mul_f32_e32 v87, 0xbfb8aa3b, v82
	v_exp_f32_e32 v87, v87
	s_nop 0
	v_add_f32_e32 v87, 1.0, v87
	v_rcp_f32_e32 v87, v87
	s_nop 0
	v_mul_f32_e32 v82, v82, v87
	v_mul_f32_e32 v82, v82, v83
	v_mul_f32_e32 v87, v82, v164
	v_mul_f32_e32 v82, 0x3c800000, v88
	v_mul_f32_e32 v83, 0xbfb8aa3b, v82
	v_exp_f32_e32 v83, v83
	s_nop 0
	v_add_f32_e32 v83, 1.0, v83
	v_rcp_f32_e32 v83, v83
	s_nop 0
	v_mul_f32_e32 v82, v82, v83
	v_mul_f32_e32 v83, 0x3c800000, v84
	v_mul_f32_e32 v82, v82, v83
	v_mul_f32_e32 v88, v82, v164
	v_mul_f32_e32 v82, 0x3c800000, v89
	v_mul_f32_e32 v83, 0xbfb8aa3b, v82
	v_exp_f32_e32 v83, v83
	s_nop 0
	v_add_f32_e32 v83, 1.0, v83
	v_rcp_f32_e32 v83, v83
	s_nop 0
	v_mul_f32_e32 v82, v82, v83
	v_mul_f32_e32 v83, 0x3c800000, v85
	v_mul_f32_e32 v82, v82, v83
	v_mul_f32_e32 v85, v82, v164
	v_cvt_pk_bf16_f32 v82, v90, v91
	v_cvt_pk_bf16_f32 v83, v92, v93
	v_cvt_pk_bf16_f32 v84, v86, v87
	v_cvt_pk_bf16_f32 v85, v88, v85
	s_mov_b64 s[0:1], exec
	s_and_b64 s[30:31], s[0:1], vcc
	v_mov_b32_e32 v218, 0x358637bd
	v_mov_b32_e32 v219, 0x43e00000
	v_mov_b32_e32 v226, 0xff800000
	v_mov_b64_e32 v[228:229], 0x1e8481
	s_mov_b64 exec, s[30:31]
	s_cbranch_execz .LBB0_1611
	v_lshlrev_b64 v[86:87], 10, v[142:143]
	v_lshl_add_u64 v[86:87], s[10:11], 0, v[86:87]
	v_lshl_add_u64 v[86:87], v[132:133], 1, v[86:87]
	s_cmp_lg_u32 s101, 0
	s_cbranch_scc1 .Lm1pl_2
	global_store_dwordx4 v[86:87], v[82:85], off sc1
	s_branch .Lm1dn_2
.Lm1pl_2:
	global_store_dwordx4 v[86:87], v[82:85], off

; __device__ __forceinline__ unsigned cvt_pk_bf16(float lo, float hi) { unsigned r; asm volatile("v_cvt_pk_bf16_f32 %0, %1, %2" : "=v"(r) : "v"(lo), "v"(hi)); return r; }
; __device__ __forceinline__ void st_wt16(void* p, u32x4 v) { asm volatile("global_store_dwordx4 %0, %1, off sc1\n\ts_nop 1" :: "v"(p), "v"(v) : "memory"); }
;     __device__ __forceinline__ void operator()(const f32x4 (&acc)[2][2][4][2], const Unit& u, int wr, int wc, int fr, int fq) const {
;     ...
;                 const int r = ai * HALF + wr * 64 + m * 16 + fr; const bool valid = r < u.rows;
;                 const int slot = slots[ai * 4 + m];
;                 const float sc = scv[ai * 4 + m], gw = gwv[ai * 4 + m]; float o[8];
; #pragma unroll
;                 for (int n = 0; n < 2; ++n) { const f32x4 g = acc[ai][0][m][n] * sc, up = acc[ai][1][m][n] * sc;
; #pragma unroll
;                     for (int j = 0; j < 4; ++j) o[4 * n + j] = g[j] * __builtin_amdgcn_rcpf(1.0f + __expf(-g[j])) * up[j] * gw; }
;                 u32x4 w; w.x = cvt_pk_bf16(o[0], o[1]); w.y = cvt_pk_bf16(o[2], o[3]); w.z = cvt_pk_bf16(o[4], o[5]); w.w = cvt_pk_bf16(o[6], o[7]);
;                 if (valid) st_wt16(hid + (size_t)slot * 512 + f0, w);
.LBB0_1611:
	s_or_b64 exec, exec, s[0:1]
	v_mul_f32_e32 v78, 0x3c800000, v78
	v_mul_f32_e32 v82, 0xbfb8aa3b, v78
	v_exp_f32_e32 v82, v82
	v_mul_f32_e32 v74, 0x3c800000, v74
	v_mul_f32_e32 v75, 0x3c800000, v75
	v_mul_f32_e32 v76, 0x3c800000, v76
	v_add_f32_e32 v82, 1.0, v82
	v_rcp_f32_e32 v82, v82
	v_mul_f32_e32 v77, 0x3c800000, v77
	v_mul_f32_e32 v70, 0x3c800000, v70
	v_mul_f32_e32 v66, 0x3c800000, v12
	v_mul_f32_e32 v78, v78, v82
	v_mul_f32_e32 v74, v78, v74
	v_mul_f32_e32 v78, 0x3c800000, v79
	v_mul_f32_e32 v79, 0xbfb8aa3b, v78
	v_exp_f32_e32 v79, v79
	v_mul_f32_e32 v67, 0x3c800000, v13
	v_cmp_gt_i32_e32 vcc, s40, v161
	s_waitcnt vmcnt(4)
	v_mul_f32_e32 v74, v74, v162
	v_add_f32_e32 v79, 1.0, v79
	v_rcp_f32_e32 v79, v79
	s_nop 0
	v_mul_f32_e32 v78, v78, v79
	v_mul_f32_e32 v75, v78, v75
	v_mul_f32_e32 v78, 0x3c800000, v80
	v_mul_f32_e32 v79, 0xbfb8aa3b, v78
	v_exp_f32_e32 v79, v79
	v_mul_f32_e32 v75, v75, v162
	v_add_f32_e32 v79, 1.0, v79
	v_rcp_f32_e32 v79, v79
	s_nop 0
	v_mul_f32_e32 v78, v78, v79
	v_mul_f32_e32 v76, v78, v76
	v_mul_f32_e32 v78, 0x3c800000, v81
	v_mul_f32_e32 v79, 0xbfb8aa3b, v78
	v_exp_f32_e32 v79, v79
	v_mul_f32_e32 v76, v76, v162
	v_add_f32_e32 v79, 1.0, v79
	v_rcp_f32_e32 v79, v79
	s_nop 0
	v_mul_f32_e32 v78, v78, v79
	v_mul_f32_e32 v77, v78, v77
	v_mul_f32_e32 v78, 0xbfb8aa3b, v70
	v_exp_f32_e32 v78, v78
	v_mul_f32_e32 v77, v77, v162
	v_add_f32_e32 v78, 1.0, v78
	v_rcp_f32_e32 v78, v78
	s_nop 0
	v_mul_f32_e32 v70, v70, v78
	v_mul_f32_e32 v66, v70, v66
	v_mul_f32_e32 v70, v66, v162
	v_mul_f32_e32 v66, 0x3c800000, v71
	v_mul_f32_e32 v71, 0xbfb8aa3b, v66
	v_exp_f32_e32 v71, v71
	s_nop 0
	v_add_f32_e32 v71, 1.0, v71
	v_rcp_f32_e32 v71, v71
	s_nop 0
	v_mul_f32_e32 v66, v66, v71
	v_mul_f32_e32 v66, v66, v67
	v_mul_f32_e32 v71, v66, v162
	v_mul_f32_e32 v66, 0x3c800000, v72
	v_mul_f32_e32 v67, 0xbfb8aa3b, v66
	v_exp_f32_e32 v67, v67
	s_nop 0
	v_add_f32_e32 v67, 1.0, v67
	v_rcp_f32_e32 v67, v67
	s_nop 0
	v_mul_f32_e32 v66, v66, v67
	v_mul_f32_e32 v67, 0x3c800000, v14
	v_mul_f32_e32 v66, v66, v67
	v_mul_f32_e32 v72, v66, v162
	v_mul_f32_e32 v66, 0x3c800000, v73
	v_mul_f32_e32 v67, 0xbfb8aa3b, v66
	v_exp_f32_e32 v67, v67
	s_nop 0
	v_add_f32_e32 v67, 1.0, v67
	v_rcp_f32_e32 v67, v67
	s_nop 0
	v_mul_f32_e32 v66, v66, v67
	v_mul_f32_e32 v67, 0x3c800000, v15
	v_mul_f32_e32 v66, v66, v67
	v_mul_f32_e32 v69, v66, v162
	v_cvt_pk_bf16_f32 v66, v74, v75
	v_cvt_pk_bf16_f32 v67, v76, v77
	v_cvt_pk_bf16_f32 v68, v70, v71
	v_cvt_pk_bf16_f32 v69, v72, v69
	s_and_saveexec_b64 s[0:1], vcc
	s_cbranch_execz .LBB0_1613
	v_lshlrev_b64 v[70:71], 10, v[140:141]
	v_lshl_add_u64 v[70:71], s[10:11], 0, v[70:71]
	v_lshl_add_u64 v[70:71], v[132:133], 1, v[70:71]
	s_cmp_lg_u32 s101, 0
	s_cbranch_scc1 .Lm1pl_3
	global_store_dwordx4 v[70:71], v[66:69], off sc1
	s_branch .Lm1dn_3
.Lm1pl_3:
	global_store_dwordx4 v[70:71], v[66:69], off

; __device__ __forceinline__ unsigned cvt_pk_bf16(float lo, float hi) { unsigned r; asm volatile("v_cvt_pk_bf16_f32 %0, %1, %2" : "=v"(r) : "v"(lo), "v"(hi)); return r; }
; __device__ __forceinline__ void st_wt16(void* p, u32x4 v) { asm volatile("global_store_dwordx4 %0, %1, off sc1\n\ts_nop 1" :: "v"(p), "v"(v) : "memory"); }
;     __device__ __forceinline__ void operator()(const f32x4 (&acc)[2][2][4][2], const Unit& u, int wr, int wc, int fr, int fq) const {
;     ...
;                 const int r = ai * HALF + wr * 64 + m * 16 + fr; const bool valid = r < u.rows;
;                 const int slot = slots[ai * 4 + m];
;                 const float sc = scv[ai * 4 + m], gw = gwv[ai * 4 + m]; float o[8];
; #pragma unroll
;                 for (int n = 0; n < 2; ++n) { const f32x4 g = acc[ai][0][m][n] * sc, up = acc[ai][1][m][n] * sc;
; #pragma unroll
;                     for (int j = 0; j < 4; ++j) o[4 * n + j] = g[j] * __builtin_amdgcn_rcpf(1.0f + __expf(-g[j])) * up[j] * gw; }
;                 u32x4 w; w.x = cvt_pk_bf16(o[0], o[1]); w.y = cvt_pk_bf16(o[2], o[3]); w.z = cvt_pk_bf16(o[4], o[5]); w.w = cvt_pk_bf16(o[6], o[7]);
;                 if (valid) st_wt16(hid + (size_t)slot * 512 + f0, w);
.LBB0_1613:
	s_or_b64 exec, exec, s[0:1]
	v_mul_f32_e32 v60, 0x3c800000, v60
	v_mul_f32_e32 v67, 0xbfb8aa3b, v60
	v_exp_f32_e32 v67, v67
	v_mul_f32_e32 v56, 0x3c800000, v56
	v_mul_f32_e32 v57, 0x3c800000, v57
	v_mul_f32_e32 v58, 0x3c800000, v58
	v_add_f32_e32 v67, 1.0, v67
	v_rcp_f32_e32 v67, v67
	v_mul_f32_e32 v59, 0x3c800000, v59
	v_mul_f32_e32 v52, 0x3c800000, v52
	v_mul_f32_e32 v48, 0x3c800000, v48
	v_mul_f32_e32 v60, v60, v67
	v_mul_f32_e32 v56, v60, v56
	v_mul_f32_e32 v60, 0x3c800000, v61
	v_mul_f32_e32 v61, 0xbfb8aa3b, v60
	v_exp_f32_e32 v61, v61
	v_mul_f32_e32 v49, 0x3c800000, v49
	v_add_u32_e32 v66, 0x80, v156
	v_cmp_gt_i32_e32 vcc, s40, v66
	v_add_f32_e32 v61, 1.0, v61
	v_rcp_f32_e32 v61, v61
	s_waitcnt vmcnt(3)
	v_mul_f32_e32 v56, v56, v160
	v_mul_f32_e32 v60, v60, v61
	v_mul_f32_e32 v57, v60, v57
	v_mul_f32_e32 v60, 0x3c800000, v62
	v_mul_f32_e32 v61, 0xbfb8aa3b, v60
	v_exp_f32_e32 v61, v61
	v_mul_f32_e32 v57, v57, v160
	v_add_f32_e32 v61, 1.0, v61
	v_rcp_f32_e32 v61, v61
	s_nop 0
	v_mul_f32_e32 v60, v60, v61
	v_mul_f32_e32 v58, v60, v58
	v_mul_f32_e32 v60, 0x3c800000, v63
	v_mul_f32_e32 v61, 0xbfb8aa3b, v60
	v_exp_f32_e32 v61, v61
	v_mul_f32_e32 v58, v58, v160
	v_add_f32_e32 v61, 1.0, v61
	v_rcp_f32_e32 v61, v61
	s_nop 0
	v_mul_f32_e32 v60, v60, v61
	v_mul_f32_e32 v59, v60, v59
	v_mul_f32_e32 v60, 0xbfb8aa3b, v52
	v_exp_f32_e32 v60, v60
	v_mul_f32_e32 v59, v59, v160
	v_add_f32_e32 v60, 1.0, v60
	v_rcp_f32_e32 v60, v60
	s_nop 0
	v_mul_f32_e32 v52, v52, v60
	v_mul_f32_e32 v48, v52, v48
	v_mul_f32_e32 v52, v48, v160
	v_mul_f32_e32 v48, 0x3c800000, v53
	v_mul_f32_e32 v53, 0xbfb8aa3b, v48
	v_exp_f32_e32 v53, v53
	s_nop 0
	v_add_f32_e32 v53, 1.0, v53
	v_rcp_f32_e32 v53, v53
	s_nop 0
	v_mul_f32_e32 v48, v48, v53
	v_mul_f32_e32 v48, v48, v49
	v_mul_f32_e32 v53, v48, v160
	v_mul_f32_e32 v48, 0x3c800000, v54
	v_mul_f32_e32 v49, 0xbfb8aa3b, v48
	v_exp_f32_e32 v49, v49
	s_nop 0
	v_add_f32_e32 v49, 1.0, v49
	v_rcp_f32_e32 v49, v49
	s_nop 0
	v_mul_f32_e32 v48, v48, v49
	v_mul_f32_e32 v49, 0x3c800000, v50
	v_mul_f32_e32 v48, v48, v49
	v_mul_f32_e32 v54, v48, v160
	v_mul_f32_e32 v48, 0x3c800000, v55
	v_mul_f32_e32 v49, 0xbfb8aa3b, v48
	v_exp_f32_e32 v49, v49
	s_nop 0
	v_add_f32_e32 v49, 1.0, v49
	v_rcp_f32_e32 v49, v49
	s_nop 0
	v_mul_f32_e32 v48, v48, v49
	v_mul_f32_e32 v49, 0x3c800000, v51
	v_mul_f32_e32 v48, v48, v49
	v_mul_f32_e32 v51, v48, v160
	v_cvt_pk_bf16_f32 v48, v56, v57
	v_cvt_pk_bf16_f32 v49, v58, v59
	v_cvt_pk_bf16_f32 v50, v52, v53
	v_cvt_pk_bf16_f32 v51, v54, v51
	s_and_saveexec_b64 s[0:1], vcc
	s_cbranch_execz .LBB0_1615
	v_lshlrev_b64 v[52:53], 10, v[138:139]
	v_lshl_add_u64 v[52:53], s[10:11], 0, v[52:53]
	v_lshl_add_u64 v[52:53], v[132:133], 1, v[52:53]
	s_cmp_lg_u32 s101, 0
	s_cbranch_scc1 .Lm1pl_4
	global_store_dwordx4 v[52:53], v[48:51], off sc1
	s_branch .Lm1dn_4
.Lm1pl_4:
	global_store_dwordx4 v[52:53], v[48:51], off

; __device__ __forceinline__ unsigned cvt_pk_bf16(float lo, float hi) { unsigned r; asm volatile("v_cvt_pk_bf16_f32 %0, %1, %2" : "=v"(r) : "v"(lo), "v"(hi)); return r; }
; __device__ __forceinline__ void st_wt16(void* p, u32x4 v) { asm volatile("global_store_dwordx4 %0, %1, off sc1\n\ts_nop 1" :: "v"(p), "v"(v) : "memory"); }
;     __device__ __forceinline__ void operator()(const f32x4 (&acc)[2][2][4][2], const Unit& u, int wr, int wc, int fr, int fq) const {
;     ...
;                 const int r = ai * HALF + wr * 64 + m * 16 + fr; const bool valid = r < u.rows;
;                 const int slot = slots[ai * 4 + m];
;                 const float sc = scv[ai * 4 + m], gw = gwv[ai * 4 + m]; float o[8];
; #pragma unroll
;                 for (int n = 0; n < 2; ++n) { const f32x4 g = acc[ai][0][m][n] * sc, up = acc[ai][1][m][n] * sc;
; #pragma unroll
;                     for (int j = 0; j < 4; ++j) o[4 * n + j] = g[j] * __builtin_amdgcn_rcpf(1.0f + __expf(-g[j])) * up[j] * gw; }
;                 u32x4 w; w.x = cvt_pk_bf16(o[0], o[1]); w.y = cvt_pk_bf16(o[2], o[3]); w.z = cvt_pk_bf16(o[4], o[5]); w.w = cvt_pk_bf16(o[6], o[7]);
;                 if (valid) st_wt16(hid + (size_t)slot * 512 + f0, w);
.LBB0_1615:
	s_or_b64 exec, exec, s[0:1]
	v_mul_f32_e32 v44, 0x3c800000, v44
	v_mul_f32_e32 v48, 0xbfb8aa3b, v44
	v_exp_f32_e32 v48, v48
	v_mul_f32_e32 v40, 0x3c800000, v40
	v_mul_f32_e32 v41, 0x3c800000, v41
	v_mul_f32_e32 v42, 0x3c800000, v42
	v_add_f32_e32 v48, 1.0, v48
	v_rcp_f32_e32 v48, v48
	v_mul_f32_e32 v43, 0x3c800000, v43
	v_mul_f32_e32 v36, 0x3c800000, v36
	v_mul_f32_e32 v32, 0x3c800000, v32
	v_mul_f32_e32 v44, v44, v48
	v_mul_f32_e32 v40, v44, v40
	v_mul_f32_e32 v44, 0x3c800000, v45
	v_mul_f32_e32 v45, 0xbfb8aa3b, v44
	v_exp_f32_e32 v45, v45
	v_mul_f32_e32 v33, 0x3c800000, v33
	s_waitcnt vmcnt(2)
	v_mul_f32_e32 v40, v40, v159
	v_add_f32_e32 v45, 1.0, v45
	v_rcp_f32_e32 v45, v45
	s_nop 0
	v_mul_f32_e32 v44, v44, v45
	v_mul_f32_e32 v41, v44, v41
	v_mul_f32_e32 v44, 0x3c800000, v46
	v_mul_f32_e32 v45, 0xbfb8aa3b, v44
	v_exp_f32_e32 v45, v45
	v_mul_f32_e32 v41, v41, v159
	v_add_f32_e32 v45, 1.0, v45
	v_rcp_f32_e32 v45, v45
	s_nop 0
	v_mul_f32_e32 v44, v44, v45
	v_mul_f32_e32 v42, v44, v42
	v_mul_f32_e32 v44, 0x3c800000, v47
	v_mul_f32_e32 v45, 0xbfb8aa3b, v44
	v_exp_f32_e32 v45, v45
	v_mul_f32_e32 v42, v42, v159
	v_add_f32_e32 v45, 1.0, v45
	v_rcp_f32_e32 v45, v45
	s_nop 0
	v_mul_f32_e32 v44, v44, v45
	v_mul_f32_e32 v43, v44, v43
	v_mul_f32_e32 v44, 0xbfb8aa3b, v36
	v_exp_f32_e32 v44, v44
	v_mul_f32_e32 v43, v43, v159
	v_add_f32_e32 v44, 1.0, v44
	v_rcp_f32_e32 v44, v44
	s_nop 0
	v_mul_f32_e32 v36, v36, v44
	v_mul_f32_e32 v32, v36, v32
	v_mul_f32_e32 v36, v32, v159
	v_mul_f32_e32 v32, 0x3c800000, v37
	v_mul_f32_e32 v37, 0xbfb8aa3b, v32
	v_exp_f32_e32 v37, v37
	s_nop 0
	v_add_f32_e32 v37, 1.0, v37
	v_rcp_f32_e32 v37, v37
	s_nop 0
	v_mul_f32_e32 v32, v32, v37
	v_mul_f32_e32 v32, v32, v33
	v_mul_f32_e32 v37, v32, v159
	v_mul_f32_e32 v32, 0x3c800000, v38
	v_mul_f32_e32 v33, 0xbfb8aa3b, v32
	v_exp_f32_e32 v33, v33
	s_nop 0
	v_add_f32_e32 v33, 1.0, v33
	v_rcp_f32_e32 v33, v33
	s_nop 0
	v_mul_f32_e32 v32, v32, v33
	v_mul_f32_e32 v33, 0x3c800000, v34
	v_mul_f32_e32 v32, v32, v33
	v_mul_f32_e32 v38, v32, v159
	v_mul_f32_e32 v32, 0x3c800000, v39
	v_mul_f32_e32 v33, 0xbfb8aa3b, v32
	v_exp_f32_e32 v33, v33
	s_nop 0
	v_add_f32_e32 v33, 1.0, v33
	v_rcp_f32_e32 v33, v33
	s_nop 0
	v_mul_f32_e32 v32, v32, v33
	v_mul_f32_e32 v33, 0x3c800000, v35
	v_mul_f32_e32 v32, v32, v33
	v_mul_f32_e32 v35, v32, v159
	v_add_u32_e32 v32, 0x90, v156
	v_cmp_gt_i32_e32 vcc, s40, v32
	v_cvt_pk_bf16_f32 v32, v40, v41
	v_cvt_pk_bf16_f32 v33, v42, v43
	v_cvt_pk_bf16_f32 v34, v36, v37
	v_cvt_pk_bf16_f32 v35, v38, v35
	s_and_saveexec_b64 s[0:1], vcc
	s_cbranch_execz .LBB0_1617
	v_lshlrev_b64 v[36:37], 10, v[136:137]
	v_lshl_add_u64 v[36:37], s[10:11], 0, v[36:37]
	v_lshl_add_u64 v[36:37], v[132:133], 1, v[36:37]
	s_cmp_lg_u32 s101, 0
	s_cbranch_scc1 .Lm1pl_5
	global_store_dwordx4 v[36:37], v[32:35], off sc1
	s_branch .Lm1dn_5
.Lm1pl_5:
	global_store_dwordx4 v[36:37], v[32:35], off

; __device__ __forceinline__ unsigned cvt_pk_bf16(float lo, float hi) { unsigned r; asm volatile("v_cvt_pk_bf16_f32 %0, %1, %2" : "=v"(r) : "v"(lo), "v"(hi)); return r; }
; __device__ __forceinline__ void st_wt16(void* p, u32x4 v) { asm volatile("global_store_dwordx4 %0, %1, off sc1\n\ts_nop 1" :: "v"(p), "v"(v) : "memory"); }
;     __device__ __forceinline__ void operator()(const f32x4 (&acc)[2][2][4][2], const Unit& u, int wr, int wc, int fr, int fq) const {
;     ...
;                 const int r = ai * HALF + wr * 64 + m * 16 + fr; const bool valid = r < u.rows;
;                 const int slot = slots[ai * 4 + m];
;                 const float sc = scv[ai * 4 + m], gw = gwv[ai * 4 + m]; float o[8];
; #pragma unroll
;                 for (int n = 0; n < 2; ++n) { const f32x4 g = acc[ai][0][m][n] * sc, up = acc[ai][1][m][n] * sc;
; #pragma unroll
;                     for (int j = 0; j < 4; ++j) o[4 * n + j] = g[j] * __builtin_amdgcn_rcpf(1.0f + __expf(-g[j])) * up[j] * gw; }
;                 u32x4 w; w.x = cvt_pk_bf16(o[0], o[1]); w.y = cvt_pk_bf16(o[2], o[3]); w.z = cvt_pk_bf16(o[4], o[5]); w.w = cvt_pk_bf16(o[6], o[7]);
;                 if (valid) st_wt16(hid + (size_t)slot * 512 + f0, w);
.LBB0_1617:
	s_or_b64 exec, exec, s[0:1]
	v_mul_f32_e32 v24, 0x3c800000, v24
	v_mul_f32_e32 v32, 0xbfb8aa3b, v24
	v_exp_f32_e32 v32, v32
	v_mul_f32_e32 v28, 0x3c800000, v28
	v_mul_f32_e32 v25, 0x3c800000, v25
	v_mul_f32_e32 v26, 0x3c800000, v26
	v_add_f32_e32 v32, 1.0, v32
	v_rcp_f32_e32 v32, v32
	v_mul_f32_e32 v27, 0x3c800000, v27
	v_mul_f32_e32 v16, 0x3c800000, v16
	v_mul_f32_e32 v20, 0x3c800000, v20
	v_mul_f32_e32 v24, v24, v32
	v_mul_f32_e32 v24, v24, v28
	v_mul_f32_e32 v28, 0xbfb8aa3b, v25
	v_exp_f32_e32 v28, v28
	s_waitcnt vmcnt(1)
	v_mul_f32_e32 v24, v24, v158
	v_add_f32_e32 v28, 1.0, v28
	v_rcp_f32_e32 v28, v28
	s_nop 0
	v_mul_f32_e32 v25, v25, v28
	v_mul_f32_e32 v28, 0x3c800000, v29
	v_mul_f32_e32 v25, v25, v28
	v_mul_f32_e32 v28, 0xbfb8aa3b, v26
	v_exp_f32_e32 v28, v28
	v_mul_f32_e32 v25, v25, v158
	v_add_f32_e32 v28, 1.0, v28
	v_rcp_f32_e32 v28, v28
	s_nop 0
	v_mul_f32_e32 v26, v26, v28
	v_mul_f32_e32 v28, 0x3c800000, v30
	v_mul_f32_e32 v26, v26, v28
	v_mul_f32_e32 v28, 0xbfb8aa3b, v27
	v_exp_f32_e32 v28, v28
	v_mul_f32_e32 v26, v26, v158
	v_add_f32_e32 v28, 1.0, v28
	v_rcp_f32_e32 v28, v28
	s_nop 0
	v_mul_f32_e32 v27, v27, v28
	v_mul_f32_e32 v28, 0x3c800000, v31
	v_mul_f32_e32 v27, v27, v28
	v_mul_f32_e32 v28, 0xbfb8aa3b, v16
	v_exp_f32_e32 v28, v28
	v_mul_f32_e32 v27, v27, v158
	v_add_f32_e32 v28, 1.0, v28
	v_rcp_f32_e32 v28, v28
	s_nop 0
	v_mul_f32_e32 v16, v16, v28
	v_mul_f32_e32 v16, v16, v20
	v_mul_f32_e32 v20, v16, v158
	v_mul_f32_e32 v16, 0x3c800000, v17
	v_mul_f32_e32 v17, 0xbfb8aa3b, v16
	v_exp_f32_e32 v17, v17
	s_nop 0
	v_add_f32_e32 v17, 1.0, v17
	v_rcp_f32_e32 v17, v17
	s_nop 0
	v_mul_f32_e32 v16, v16, v17
	v_mul_f32_e32 v17, 0x3c800000, v21
	v_mul_f32_e32 v16, v16, v17
	v_mul_f32_e32 v21, v16, v158
	v_mul_f32_e32 v16, 0x3c800000, v18
	v_mul_f32_e32 v17, 0xbfb8aa3b, v16
	v_exp_f32_e32 v17, v17
	s_nop 0
	v_add_f32_e32 v17, 1.0, v17
	v_rcp_f32_e32 v17, v17
	s_nop 0
	v_mul_f32_e32 v16, v16, v17
	v_mul_f32_e32 v17, 0x3c800000, v22
	v_mul_f32_e32 v16, v16, v17
	v_mul_f32_e32 v22, v16, v158
	v_mul_f32_e32 v16, 0x3c800000, v19
	v_mul_f32_e32 v17, 0xbfb8aa3b, v16
	v_exp_f32_e32 v17, v17
	s_nop 0
	v_add_f32_e32 v17, 1.0, v17
	v_rcp_f32_e32 v17, v17
	s_nop 0
	v_mul_f32_e32 v16, v16, v17
	v_mul_f32_e32 v17, 0x3c800000, v23
	v_mul_f32_e32 v16, v16, v17
	v_mul_f32_e32 v19, v16, v158
	v_add_u32_e32 v16, 0xa0, v156
	v_cmp_gt_i32_e32 vcc, s40, v16
	v_cvt_pk_bf16_f32 v16, v24, v25
	v_cvt_pk_bf16_f32 v17, v26, v27
	v_cvt_pk_bf16_f32 v18, v20, v21
	v_cvt_pk_bf16_f32 v19, v22, v19
	s_and_saveexec_b64 s[0:1], vcc
	s_cbranch_execz .LBB0_1619
	v_lshlrev_b64 v[20:21], 10, v[134:135]
	v_lshl_add_u64 v[20:21], s[10:11], 0, v[20:21]
	v_lshl_add_u64 v[20:21], v[132:133], 1, v[20:21]
	s_cmp_lg_u32 s101, 0
	s_cbranch_scc1 .Lm1pl_6
	global_store_dwordx4 v[20:21], v[16:19], off sc1
	s_branch .Lm1dn_6
.Lm1pl_6:
	global_store_dwordx4 v[20:21], v[16:19], off

; __device__ __forceinline__ unsigned cvt_pk_bf16(float lo, float hi) { unsigned r; asm volatile("v_cvt_pk_bf16_f32 %0, %1, %2" : "=v"(r) : "v"(lo), "v"(hi)); return r; }
; __device__ __forceinline__ void st_wt16(void* p, u32x4 v) { asm volatile("global_store_dwordx4 %0, %1, off sc1\n\ts_nop 1" :: "v"(p), "v"(v) : "memory"); }
;     __device__ __forceinline__ void operator()(const f32x4 (&acc)[2][2][4][2], const Unit& u, int wr, int wc, int fr, int fq) const {
;     ...
;                 const int r = ai * HALF + wr * 64 + m * 16 + fr; const bool valid = r < u.rows;
;                 const int slot = slots[ai * 4 + m];
;                 const float sc = scv[ai * 4 + m], gw = gwv[ai * 4 + m]; float o[8];
; #pragma unroll
;                 for (int n = 0; n < 2; ++n) { const f32x4 g = acc[ai][0][m][n] * sc, up = acc[ai][1][m][n] * sc;
; #pragma unroll
;                     for (int j = 0; j < 4; ++j) o[4 * n + j] = g[j] * __builtin_amdgcn_rcpf(1.0f + __expf(-g[j])) * up[j] * gw; }
;                 u32x4 w; w.x = cvt_pk_bf16(o[0], o[1]); w.y = cvt_pk_bf16(o[2], o[3]); w.z = cvt_pk_bf16(o[4], o[5]); w.w = cvt_pk_bf16(o[6], o[7]);
;                 if (valid) st_wt16(hid + (size_t)slot * 512 + f0, w);
.LBB0_1619:
	s_or_b64 exec, exec, s[0:1]
	v_mul_f32_e32 v8, 0x3c800000, v8
	v_mul_f32_e32 v16, 0xbfb8aa3b, v8
	v_exp_f32_e32 v16, v16
	v_mul_f32_e32 v12, 0x3c800000, v0
	v_mul_f32_e32 v9, 0x3c800000, v9
	v_mul_f32_e32 v10, 0x3c800000, v10
	v_add_f32_e32 v16, 1.0, v16
	v_rcp_f32_e32 v16, v16
	v_mul_f32_e32 v11, 0x3c800000, v11
	v_mul_f32_e32 v0, 0x3c800000, v230
	v_mul_f32_e32 v4, 0x3c800000, v4
	v_mul_f32_e32 v8, v8, v16
	v_mul_f32_e32 v8, v8, v12
	v_mul_f32_e32 v12, 0xbfb8aa3b, v9
	v_exp_f32_e32 v12, v12
	s_waitcnt vmcnt(0)
	v_mul_f32_e32 v8, v8, v157
	v_add_f32_e32 v12, 1.0, v12
	v_rcp_f32_e32 v12, v12
	s_nop 0
	v_mul_f32_e32 v9, v9, v12
	v_mul_f32_e32 v12, 0x3c800000, v1
	v_mul_f32_e32 v9, v9, v12
	v_mul_f32_e32 v12, 0xbfb8aa3b, v10
	v_exp_f32_e32 v12, v12
	v_mul_f32_e32 v9, v9, v157
	v_add_f32_e32 v12, 1.0, v12
	v_rcp_f32_e32 v12, v12
	s_nop 0
	v_mul_f32_e32 v10, v10, v12
	v_mul_f32_e32 v12, 0x3c800000, v2
	v_mul_f32_e32 v10, v10, v12
	v_mul_f32_e32 v12, 0xbfb8aa3b, v11
	v_exp_f32_e32 v12, v12
	v_mul_f32_e32 v10, v10, v157
	v_add_f32_e32 v12, 1.0, v12
	v_rcp_f32_e32 v12, v12
	s_nop 0
	v_mul_f32_e32 v11, v11, v12
	v_mul_f32_e32 v12, 0x3c800000, v3
	v_mul_f32_e32 v11, v11, v12
	v_mul_f32_e32 v12, 0xbfb8aa3b, v0
	v_exp_f32_e32 v12, v12
	v_mul_f32_e32 v11, v11, v157
	v_add_f32_e32 v12, 1.0, v12
	v_rcp_f32_e32 v12, v12
	s_nop 0
	v_mul_f32_e32 v0, v0, v12
	v_mul_f32_e32 v0, v0, v4
	v_mul_f32_e32 v4, v0, v157
	v_mul_f32_e32 v0, 0x3c800000, v231
	v_mul_f32_e32 v1, 0xbfb8aa3b, v0
	v_exp_f32_e32 v1, v1
	s_nop 0
	v_add_f32_e32 v1, 1.0, v1
	v_rcp_f32_e32 v1, v1
	s_nop 0
	v_mul_f32_e32 v0, v0, v1
	v_mul_f32_e32 v1, 0x3c800000, v5
	v_mul_f32_e32 v0, v0, v1
	v_mul_f32_e32 v5, v0, v157
	v_mul_f32_e32 v0, 0x3c800000, v232
	v_mul_f32_e32 v1, 0xbfb8aa3b, v0
	v_exp_f32_e32 v1, v1
	s_nop 0
	v_add_f32_e32 v1, 1.0, v1
	v_rcp_f32_e32 v1, v1
	s_nop 0
	v_mul_f32_e32 v0, v0, v1
	v_mul_f32_e32 v1, 0x3c800000, v6
	v_mul_f32_e32 v0, v0, v1
	v_mul_f32_e32 v6, v0, v157
	v_mul_f32_e32 v0, 0x3c800000, v233
	v_mul_f32_e32 v1, 0xbfb8aa3b, v0
	v_exp_f32_e32 v1, v1
	s_nop 0
	v_add_f32_e32 v1, 1.0, v1
	v_rcp_f32_e32 v1, v1
	s_nop 0
	v_mul_f32_e32 v0, v0, v1
	v_mul_f32_e32 v1, 0x3c800000, v7
	v_mul_f32_e32 v0, v0, v1
	v_mul_f32_e32 v3, v0, v157
	v_add_u32_e32 v0, 0xb0, v156
	v_cmp_gt_i32_e32 vcc, s40, v0
	v_cvt_pk_bf16_f32 v0, v8, v9
	v_cvt_pk_bf16_f32 v1, v10, v11
	v_cvt_pk_bf16_f32 v2, v4, v5
	v_cvt_pk_bf16_f32 v3, v6, v3
	s_and_saveexec_b64 s[0:1], vcc
	s_cbranch_execz .LBB0_1621
	v_lshlrev_b64 v[4:5], 10, v[130:131]
	v_lshl_add_u64 v[4:5], s[10:11], 0, v[4:5]
	v_lshl_add_u64 v[4:5], v[132:133], 1, v[4:5]
	s_cmp_lg_u32 s101, 0
	s_cbranch_scc1 .Lm1pl_7
	global_store_dwordx4 v[4:5], v[0:3], off sc1
	s_branch .Lm1dn_7
.Lm1pl_7:
	global_store_dwordx4 v[4:5], v[0:3], off

;     __device__ __forceinline__ bool next(int i, Unit& u) const {
;         const int T = __builtin_amdgcn_readfirstlane(moe[16]), Ng = (T + 7) >> 3, x = c & 7, k = c >> 3; int g;
;         if (TOKEN_ROWS) g = x + 8 * i;
;         else { const int hc = Ng & 7, nl = 8 - hc;
;             if (x >= hc) g = i == 0 ? x - hc : nl + (i - 1) * 8 + (x - hc); else g = 2 * nl + 8 * i + x; }
;         if (g >= Ng) return false;
;         const int rt = g * 8 + (k >> 2); if (rt >= T) return false;
;         u.pn = k & 3; int e = 0;
; #pragma unroll
;         for (int j = 1; j < 16; ++j) e = (rt >= moe[j]) ? j : e;
;         e = __builtin_amdgcn_readfirstlane(e);
;         u.e = e; u.pm = __builtin_amdgcn_readfirstlane(rt - moe[e]); const int left = __builtin_amdgcn_readfirstlane(moe[17 + e]) - u.pm * BM; u.rows = left < BM ? left : BM; return true;
.LBB0_1628:
	v_mbcnt_lo_u32_b32 v0, -1, 0
	v_mbcnt_hi_u32_b32 v0, -1, v0
	v_readlane_b32 s0, v254, 37
	v_add_u32_e32 v2, s93, v0
	s_or_b32 s33, s42, 16
	v_mov_b32_e32 v0, s0
	ds_read_b32 v0, v0
	v_readfirstlane_b32 s16, v2
	s_waitcnt lgkmcnt(0)
	v_readfirstlane_b32 s4, v0
	s_add_i32 s0, s4, 7
	s_ashr_i32 s2, s0, 3
	s_and_b32 s0, s2, 7
	s_lshr_b32 s3, s2, 3
	s_sub_i32 s1, 7, s42
	s_cmp_lt_u32 s1, s0
	s_cselect_b32 s1, s1, s2
	s_cmp_eq_u32 s3, 0
	s_cselect_b32 s1, s1, s42
	s_cmp_ge_i32 s1, s2
	s_mov_b64 s[2:3], 0
	s_cbranch_scc1 .LBB0_1631
	s_lshl_b32 s1, s1, 3
	s_ashr_i32 s0, s36, 5
	s_add_i32 s1, s1, s0
	s_cmp_ge_i32 s1, s4
	s_cbranch_scc1 .LBB0_1631
	v_readlane_b32 s2, v254, 29
	s_bfe_u32 s0, s36, 0x20003
	s_nop 0
	v_mov_b32_e32 v0, s2
	ds_read_b128 v[16:19], v0
	ds_read_b128 v[20:23], v0 offset:16
	ds_read_b128 v[24:27], v0 offset:32
	ds_read_b128 v[28:31], v0 offset:48
	s_mov_b32 s20, 0
	s_waitcnt lgkmcnt(0)
	v_readfirstlane_b32 s2, v17
	s_cmp_ge_i32 s1, s2
	s_addc_u32 s20, s20, 0
	v_readfirstlane_b32 s2, v18
	s_cmp_ge_i32 s1, s2
	s_addc_u32 s20, s20, 0
	v_readfirstlane_b32 s2, v19
	s_cmp_ge_i32 s1, s2
	s_addc_u32 s20, s20, 0
	v_readfirstlane_b32 s2, v20
	s_cmp_ge_i32 s1, s2
	s_addc_u32 s20, s20, 0
	v_readfirstlane_b32 s2, v21
	s_cmp_ge_i32 s1, s2
	s_addc_u32 s20, s20, 0
	v_readfirstlane_b32 s2, v22
	s_cmp_ge_i32 s1, s2
	s_addc_u32 s20, s20, 0
	v_readfirstlane_b32 s2, v23
	s_cmp_ge_i32 s1, s2
	s_addc_u32 s20, s20, 0
	v_readfirstlane_b32 s2, v24
	s_cmp_ge_i32 s1, s2
	s_addc_u32 s20, s20, 0
	v_readfirstlane_b32 s2, v25
	s_cmp_ge_i32 s1, s2
	s_addc_u32 s20, s20, 0
	v_readfirstlane_b32 s2, v26
	s_cmp_ge_i32 s1, s2
	s_addc_u32 s20, s20, 0
	v_readfirstlane_b32 s2, v27
	s_cmp_ge_i32 s1, s2
	s_addc_u32 s20, s20, 0
	v_readfirstlane_b32 s2, v28
	s_cmp_ge_i32 s1, s2
	s_addc_u32 s20, s20, 0
	v_readfirstlane_b32 s2, v29
	s_cmp_ge_i32 s1, s2
	s_addc_u32 s20, s20, 0
	v_readfirstlane_b32 s2, v30
	s_cmp_ge_i32 s1, s2
	s_addc_u32 s20, s20, 0
	v_readfirstlane_b32 s2, v31
	s_cmp_ge_i32 s1, s2
	s_addc_u32 s20, s20, 0
	s_lshl_b32 s2, s20, 2
	s_addk_i32 s2, 0x100
	s_add_i32 s2, s2, 0x20040
	v_mov_b32_e32 v0, s2
	ds_read2_b32 v[0:1], v0 offset1:17
	s_waitcnt lgkmcnt(0)
	v_sub_u32_e32 v0, s1, v0
	s_nop 0
	v_readfirstlane_b32 s63, v0
	v_readfirstlane_b32 s1, v1
	s_lshl_b32 s2, s63, 8
	s_sub_i32 s1, s1, s2
	s_min_i32 s38, s1, 0x100
	s_mov_b64 s[2:3], -1

;     __device__ __forceinline__ bool next(int i, Unit& u) const {
;         const int T = __builtin_amdgcn_readfirstlane(moe[16]), Ng = (T + 7) >> 3, x = c & 7, k = c >> 3; int g;
;         if (TOKEN_ROWS) g = x + 8 * i;
;         else { const int hc = Ng & 7, nl = 8 - hc;
;             if (x >= hc) g = i == 0 ? x - hc : nl + (i - 1) * 8 + (x - hc); else g = 2 * nl + 8 * i + x; }
;         if (g >= Ng) return false;
;         const int rt = g * 8 + (k >> 2); if (rt >= T) return false;
;         u.pn = k & 3; int e = 0;
; #pragma unroll
;         for (int j = 1; j < 16; ++j) e = (rt >= moe[j]) ? j : e;
;         e = __builtin_amdgcn_readfirstlane(e);
;         u.e = e; u.pm = __builtin_amdgcn_readfirstlane(rt - moe[e]); const int left = __builtin_amdgcn_readfirstlane(moe[17 + e]) - u.pm * BM; u.rows = left < BM ? left : BM; return true;
;     ...
;         const bool has_next = S.next(ui + 1, nxt);
.LBB0_1652:
	v_readlane_b32 s1, v254, 37
	s_add_i32 s62, s62, 1
	s_mov_b64 s[28:29], 0
	v_mov_b32_e32 v0, s1
	ds_read_b32 v0, v0
	s_lshl_b32 s1, s62, 3
	s_add_i32 s5, s1, s33
	s_or_b32 s1, s1, s42
	s_waitcnt lgkmcnt(0)
	v_readfirstlane_b32 s4, v0
	s_add_i32 s6, s4, 7
	s_ashr_i32 s6, s6, 3
	s_and_b32 s7, s6, 7
	s_lshr_b32 s19, s6, 3
	s_sub_i32 s5, 7, s42
	s_cmp_lt_u32 s5, s7
	s_cselect_b32 s7, 0, 1
	s_lshl3_add_u32 s5, s19, s5
	s_cmp_lg_u32 s7, 0
	s_cselect_b32 s5, s6, s5
	s_cmp_lt_u32 s62, s19
	s_cselect_b32 s1, s1, s5
	s_cmp_gt_u32 s62, s19
	s_cselect_b32 s1, s6, s1
	s_cmp_ge_i32 s1, s6
	s_cbranch_scc1 .LBB0_1655
	s_lshl_b32 s1, s1, 3
	s_add_i32 s1, s1, s61
	s_mov_b32 s101, s1
	s_cmp_ge_i32 s1, s4
	s_cbranch_scc1 .LBB0_1655
	v_readlane_b32 s4, v254, 29
	s_mov_b64 s[28:29], -1
	s_nop 0
	v_mov_b32_e32 v0, s4
	ds_read_b128 v[16:19], v0
	ds_read_b128 v[20:23], v0 offset:16
	ds_read_b128 v[24:27], v0 offset:32
	ds_read_b128 v[28:31], v0 offset:48
	s_mov_b32 s22, 0
	s_waitcnt lgkmcnt(0)
	v_readfirstlane_b32 s4, v17
	s_cmp_ge_i32 s1, s4
	s_addc_u32 s22, s22, 0
	v_readfirstlane_b32 s4, v18
	s_cmp_ge_i32 s1, s4
	s_addc_u32 s22, s22, 0
	v_readfirstlane_b32 s4, v19
	s_cmp_ge_i32 s1, s4
	s_addc_u32 s22, s22, 0
	v_readfirstlane_b32 s4, v20
	s_cmp_ge_i32 s1, s4
	s_addc_u32 s22, s22, 0
	v_readfirstlane_b32 s4, v21
	s_cmp_ge_i32 s1, s4
	s_addc_u32 s22, s22, 0
	v_readfirstlane_b32 s4, v22
	s_cmp_ge_i32 s1, s4
	s_addc_u32 s22, s22, 0
	v_readfirstlane_b32 s4, v23
	s_cmp_ge_i32 s1, s4
	s_addc_u32 s22, s22, 0
	v_readfirstlane_b32 s4, v24
	s_cmp_ge_i32 s1, s4
	s_addc_u32 s22, s22, 0
	v_readfirstlane_b32 s4, v25
	s_cmp_ge_i32 s1, s4
	s_addc_u32 s22, s22, 0
	v_readfirstlane_b32 s4, v26
	s_cmp_ge_i32 s1, s4
	s_addc_u32 s22, s22, 0
	v_readfirstlane_b32 s4, v27
	s_cmp_ge_i32 s1, s4
	s_addc_u32 s22, s22, 0
	v_readfirstlane_b32 s4, v28
	s_cmp_ge_i32 s1, s4
	s_addc_u32 s22, s22, 0
	v_readfirstlane_b32 s4, v29
	s_cmp_ge_i32 s1, s4
	s_addc_u32 s22, s22, 0
	v_readfirstlane_b32 s4, v30
	s_cmp_ge_i32 s1, s4
	s_addc_u32 s22, s22, 0
	v_readfirstlane_b32 s4, v31
	s_cmp_ge_i32 s1, s4
	s_addc_u32 s22, s22, 0
	s_lshl_b32 s4, s22, 2
	s_addk_i32 s4, 0x100
	s_add_i32 s4, s4, 0x20040
	v_mov_b32_e32 v0, s4
	ds_read2_b32 v[0:1], v0 offset1:17
	s_waitcnt lgkmcnt(0)
	v_sub_u32_e32 v0, s1, v0
	s_nop 0
	v_readfirstlane_b32 s64, v0
	v_readfirstlane_b32 s1, v1
	s_lshl_b32 s4, s64, 8
	s_sub_i32 s1, s1, s4
	s_min_i32 s65, s1, 0x100
